# P0 transposes: fp8 output stores of item i deferred behind item i+1's first load batch; per-wave kscale rows loaded once (k-block is invariant per wave)
# baseline (speedup 1.0000x reference)
.LBB0_8:
	s_or_b64 exec, exec, s[2:3]
	s_ashr_i32 s0, s0, 6
	s_lshl_b32 s1, s82, 3
	s_add_i32 s14, s0, s1
	s_waitcnt lgkmcnt(0)
	s_add_u32 s18, s12, 0x1a00000
	s_addc_u32 s19, s13, 0
	s_lshl_b32 s80, s88, 3
	s_mov_b32 s60, 0
	s_mov_b32 s61, 0
	s_cmp_gt_i32 s14, 0xc4ff
	v_and_b32_e32 v36, 63, v37
	v_writelane_b32 v254, s1, 5
	s_cbranch_scc1 .LBB0_31
	s_add_u32 s1, s12, 0x1c00000
	s_addc_u32 s2, s13, 0
	v_lshlrev_b32_e32 v1, 4, v36
	s_add_u32 s3, s12, 0x5c00000
	s_mul_i32 s4, s0, 0x2100
	v_and_b32_e32 v10, 48, v1
	s_addc_u32 s11, s13, 0
	s_add_i32 s4, s4, 0
	v_mul_u32_u24_e32 v1, 0x84, v10
	v_and_b32_e32 v3, 60, v36
	v_add3_u32 v7, s4, v1, v3
	v_lshlrev_b32_e32 v1, 2, v36
	v_lshrrev_b32_e32 v5, 2, v36
	v_and_b32_e32 v1, 0x80, v1
	v_and_or_b32 v9, v5, 7, v1
	v_lshlrev_b32_e32 v1, 3, v36
	v_lshrrev_b32_e32 v24, 3, v36
	v_and_b32_e32 v1, 56, v1
	v_and_b32_e32 v6, 31, v37
	v_mov_b32_e32 v13, 0
	v_mul_u32_u24_e32 v3, 0x84, v1
	v_lshlrev_b32_e32 v12, 1, v1
	v_lshlrev_b32_e32 v1, 2, v24
	v_lshrrev_b32_e32 v4, 5, v36
	v_lshl_add_u32 v8, v6, 2, s4
	v_add3_u32 v25, s4, v3, v1
	v_lshl_add_u64 v[16:17], s[12:13], 0, v[12:13]
	s_mov_b64 s[4:5], 0x1600000
	s_mov_b32 s9, 0
	s_movk_i32 s15, 0x84
	v_mov_b32_e32 v11, v13
	v_or_b32_e32 v21, 16, v5
	v_lshl_add_u64 v[14:15], s[18:19], 0, v[12:13]
	v_or_b32_e32 v26, 8, v24
	v_or_b32_e32 v27, 16, v24
	v_or_b32_e32 v28, 24, v24
	v_lshl_add_u64 v[16:17], v[16:17], 0, s[4:5]
	v_mov_b32_e32 v1, v4
	s_brev_b32 s10, 34
	s_movk_i32 s24, 0x7fff
	s_mov_b32 s25, 0xffff0000
	v_mov_b32_e32 v29, 0x2000
	s_mov_b32 s26, s14
	s_branch .LBB0_11

.LBB0_16:
	v_readfirstlane_b32 s50, v18
	s_lshl_b32 s51, s8, 12
	s_lshl_b32 s50, s50, 2
	s_add_u32 s50, s50, s51
	s_add_u32 s56, s6, s50
	s_addc_u32 s57, s7, 0
	v_and_b32_e32 v100, 3, v36
	v_lshrrev_b32_e32 v101, 5, v36
	v_lshl_or_b32 v100, v101, 2, v100
	v_bfe_u32 v101, v36, 2, 3
	v_lshlrev_b32_e32 v102, 12, v100
	v_lshl_or_b32 v102, v101, 4, v102
	v_lshlrev_b32_e32 v103, 2, v6
	v_sub_u32_e32 v103, v8, v103
	v_mad_u32_u24 v103, v100, s15, v103
	v_lshl_add_u32 v103, v101, 4, v103
	global_load_dwordx4 v[120:123], v102, s[56:57]
	s_add_u32 s56, s56, 0x8000
	s_addc_u32 s57, s57, 0
	global_load_dwordx4 v[124:127], v102, s[56:57]
	s_add_u32 s56, s56, 0x8000
	s_addc_u32 s57, s57, 0
	s_cmp_lg_u32 s60, 0
	s_cbranch_scc0 .Lnp_dn
	global_store_dwordx4 v[164:165], v[160:163], off
	global_store_dwordx4 v[170:171], v[166:169], off
	s_waitcnt vmcnt(2)
	s_branch .Ljoin_dn

.Ljoin_dn:
	v_pk_mul_f32 v[120:121], v[120:121], s[10:11] op_sel_hi:[1,0]
	v_pk_mul_f32 v[122:123], v[122:123], s[10:11] op_sel_hi:[1,0]
	ds_write_b32 v103, v120 offset:0
	ds_write_b32 v103, v121 offset:4
	ds_write_b32 v103, v122 offset:8
	ds_write_b32 v103, v123 offset:12
	v_pk_mul_f32 v[124:125], v[124:125], s[10:11] op_sel_hi:[1,0]
	v_pk_mul_f32 v[126:127], v[126:127], s[10:11] op_sel_hi:[1,0]
	ds_write_b32 v103, v124 offset:1056
	ds_write_b32 v103, v125 offset:1060
	ds_write_b32 v103, v126 offset:1064
	ds_write_b32 v103, v127 offset:1068
	global_load_dwordx4 v[128:131], v102, s[56:57]
	s_add_u32 s56, s56, 0x8000
	s_addc_u32 s57, s57, 0
	global_load_dwordx4 v[132:135], v102, s[56:57]
	s_add_u32 s56, s56, 0x8000
	s_addc_u32 s57, s57, 0
	s_waitcnt vmcnt(1)
	v_pk_mul_f32 v[128:129], v[128:129], s[10:11] op_sel_hi:[1,0]
	v_pk_mul_f32 v[130:131], v[130:131], s[10:11] op_sel_hi:[1,0]
	ds_write_b32 v103, v128 offset:2112
	ds_write_b32 v103, v129 offset:2116
	ds_write_b32 v103, v130 offset:2120
	ds_write_b32 v103, v131 offset:2124
	s_waitcnt vmcnt(0)
	v_pk_mul_f32 v[132:133], v[132:133], s[10:11] op_sel_hi:[1,0]
	v_pk_mul_f32 v[134:135], v[134:135], s[10:11] op_sel_hi:[1,0]
	ds_write_b32 v103, v132 offset:3168
	ds_write_b32 v103, v133 offset:3172
	ds_write_b32 v103, v134 offset:3176
	ds_write_b32 v103, v135 offset:3180
	global_load_dwordx4 v[136:139], v102, s[56:57]
	s_add_u32 s56, s56, 0x8000
	s_addc_u32 s57, s57, 0
	global_load_dwordx4 v[140:143], v102, s[56:57]
	s_add_u32 s56, s56, 0x8000
	s_addc_u32 s57, s57, 0
	s_waitcnt vmcnt(1)
	v_pk_mul_f32 v[136:137], v[136:137], s[10:11] op_sel_hi:[1,0]
	v_pk_mul_f32 v[138:139], v[138:139], s[10:11] op_sel_hi:[1,0]
	ds_write_b32 v103, v136 offset:4224
	ds_write_b32 v103, v137 offset:4228
	ds_write_b32 v103, v138 offset:4232
	ds_write_b32 v103, v139 offset:4236
	s_waitcnt vmcnt(0)
	v_pk_mul_f32 v[140:141], v[140:141], s[10:11] op_sel_hi:[1,0]
	v_pk_mul_f32 v[142:143], v[142:143], s[10:11] op_sel_hi:[1,0]
	ds_write_b32 v103, v140 offset:5280
	ds_write_b32 v103, v141 offset:5284
	ds_write_b32 v103, v142 offset:5288
	ds_write_b32 v103, v143 offset:5292
	global_load_dwordx4 v[144:147], v102, s[56:57]
	s_add_u32 s56, s56, 0x8000
	s_addc_u32 s57, s57, 0
	global_load_dwordx4 v[148:151], v102, s[56:57]
	s_add_u32 s56, s56, 0x8000
	s_addc_u32 s57, s57, 0
	s_waitcnt vmcnt(1)
	v_pk_mul_f32 v[144:145], v[144:145], s[10:11] op_sel_hi:[1,0]
	v_pk_mul_f32 v[146:147], v[146:147], s[10:11] op_sel_hi:[1,0]
	ds_write_b32 v103, v144 offset:6336
	ds_write_b32 v103, v145 offset:6340
	ds_write_b32 v103, v146 offset:6344
	ds_write_b32 v103, v147 offset:6348
	s_waitcnt vmcnt(0)
	v_pk_mul_f32 v[148:149], v[148:149], s[10:11] op_sel_hi:[1,0]
	v_pk_mul_f32 v[150:151], v[150:151], s[10:11] op_sel_hi:[1,0]
	ds_write_b32 v103, v148 offset:7392
	ds_write_b32 v103, v149 offset:7396
	ds_write_b32 v103, v150 offset:7400
	ds_write_b32 v103, v151 offset:7404
	s_waitcnt lgkmcnt(0)
	v_add_u32_e32 v12, 0x400, v7
	ds_read2_b32 v[22:23], v7 offset1:16
	ds_read2_b32 v[34:35], v7 offset0:33 offset1:49
	ds_read2_b32 v[38:39], v7 offset0:66 offset1:82
	ds_read2_b32 v[40:41], v7 offset0:99 offset1:115
	ds_read2_b32 v[42:43], v7 offset0:132 offset1:148
	ds_read2_b32 v[44:45], v7 offset0:165 offset1:181
	ds_read2_b32 v[46:47], v7 offset0:198 offset1:214
	ds_read2_b32 v[48:49], v7 offset0:231 offset1:247
	ds_read2_b32 v[50:51], v12 offset0:8 offset1:24
	ds_read2_b32 v[52:53], v12 offset0:41 offset1:57
	ds_read2_b32 v[54:55], v12 offset0:74 offset1:90
	ds_read2_b32 v[56:57], v12 offset0:107 offset1:123
	ds_read2_b32 v[58:59], v12 offset0:140 offset1:156
	ds_read2_b32 v[60:61], v12 offset0:173 offset1:189
	s_add_u32 s4, s1, s4
	ds_read2_b32 v[62:63], v12 offset0:206 offset1:222
	ds_read2_b32 v[64:65], v12 offset0:239 offset1:255
	s_addc_u32 s5, s2, s5
	s_lshl_b32 s7, s20, 4
	s_waitcnt lgkmcnt(14)
	v_cvt_pk_fp8_f32 v30, v22, v34
	s_waitcnt lgkmcnt(10)
	v_cvt_pk_fp8_f32 v31, v42, v44
	s_waitcnt lgkmcnt(6)
	v_cvt_pk_fp8_f32 v32, v50, v52
	s_waitcnt lgkmcnt(2)
	v_cvt_pk_fp8_f32 v33, v58, v60
	s_and_b32 s6, s21, 0x300
	s_and_b32 s20, s7, 0x60
	s_add_u32 s4, s4, s8
	v_or_b32_e32 v3, s6, v9
	s_addc_u32 s5, s5, 0
	v_or_b32_e32 v3, s20, v3
	v_lshl_add_u64 v[18:19], s[4:5], 0, v[10:11]
	s_and_b32 s4, s7, 16
	v_cvt_pk_fp8_f32 v30, v38, v40 op_sel:[0,0,1]
	v_cvt_pk_fp8_f32 v31, v46, v48 op_sel:[0,0,1]
	v_cvt_pk_fp8_f32 v32, v54, v56 op_sel:[0,0,1]
	s_waitcnt lgkmcnt(0)
	v_cvt_pk_fp8_f32 v33, v62, v64 op_sel:[0,0,1]
	v_or_b32_e32 v12, s4, v3
	v_lshlrev_b32_e32 v12, 10, v12
	v_lshl_add_u64 v[66:67], v[18:19], 0, v[12:13]
	v_mov_b32_e32 v160, v30
	v_mov_b32_e32 v161, v31
	v_mov_b32_e32 v162, v32
	v_mov_b32_e32 v163, v33
	v_mov_b32_e32 v164, v66
	v_mov_b32_e32 v165, v67
	v_add_u32_e32 v3, s4, v3
	v_lshl_add_u32 v12, v3, 10, v29
	v_cvt_pk_fp8_f32 v30, v23, v35
	v_cvt_pk_fp8_f32 v31, v43, v45
	v_cvt_pk_fp8_f32 v32, v51, v53
	v_cvt_pk_fp8_f32 v33, v59, v61
	v_cvt_pk_fp8_f32 v30, v39, v41 op_sel:[0,0,1]
	v_cvt_pk_fp8_f32 v31, v47, v49 op_sel:[0,0,1]
	v_cvt_pk_fp8_f32 v32, v55, v57 op_sel:[0,0,1]
	v_cvt_pk_fp8_f32 v33, v63, v65 op_sel:[0,0,1]
	v_lshl_add_u64 v[18:19], v[18:19], 0, v[12:13]
	s_mov_b64 s[4:5], 0
	v_mov_b32_e32 v166, v30
	v_mov_b32_e32 v167, v31
	v_mov_b32_e32 v168, v32
	v_mov_b32_e32 v169, v33
	v_mov_b32_e32 v170, v18
	v_mov_b32_e32 v171, v19
	s_mov_b32 s60, 1
	s_waitcnt lgkmcnt(0)

.LBB0_20:
	v_readfirstlane_b32 s56, v18
	v_readfirstlane_b32 s57, v19
	s_lshl_b32 s51, s6, 13
	s_add_u32 s56, s56, s51
	s_addc_u32 s57, s57, 0
	s_lshl_b32 s52, s6, 2
	s_add_u32 s52, s4, s52
	s_addc_u32 s53, s5, 0
	v_and_b32_e32 v100, 3, v36
	v_lshrrev_b32_e32 v101, 5, v36
	v_lshl_or_b32 v100, v101, 2, v100
	v_bfe_u32 v101, v36, 2, 3
	v_lshlrev_b32_e32 v102, 13, v100
	v_lshl_or_b32 v102, v101, 4, v102
	v_lshlrev_b32_e32 v104, 2, v100
	v_lshlrev_b32_e32 v103, 2, v6
	v_sub_u32_e32 v103, v8, v103
	v_mad_u32_u24 v103, v100, s15, v103
	v_lshl_add_u32 v103, v101, 4, v103
	s_cmp_lg_u32 s61, 0
	s_cbranch_scc1 .Lks_done
	global_load_dword v152, v104, s[52:53] offset:0
	global_load_dword v153, v104, s[52:53] offset:32
	global_load_dword v154, v104, s[52:53] offset:64
	global_load_dword v155, v104, s[52:53] offset:96
	global_load_dword v156, v104, s[52:53] offset:128
	global_load_dword v157, v104, s[52:53] offset:160
	global_load_dword v158, v104, s[52:53] offset:192
	global_load_dword v159, v104, s[52:53] offset:224
	s_waitcnt vmcnt(0)
	s_mov_b32 s61, 1
.Lks_done:
	global_load_dwordx4 v[120:123], v102, s[56:57]
	s_add_u32 s56, s56, 0x10000
	s_addc_u32 s57, s57, 0
	global_load_dwordx4 v[124:127], v102, s[56:57]
	s_add_u32 s56, s56, 0x10000
	s_addc_u32 s57, s57, 0
	s_cmp_lg_u32 s60, 0
	s_cbranch_scc0 .Lnp_gu
	global_store_dwordx4 v[164:165], v[160:163], off
	global_store_dwordx4 v[170:171], v[166:169], off
	s_waitcnt vmcnt(2)
	s_branch .Ljoin_gu

.Ljoin_gu:
	v_pk_mul_f32 v[120:121], v[120:121], s[10:11] op_sel_hi:[1,0]
	v_pk_mul_f32 v[122:123], v[122:123], s[10:11] op_sel_hi:[1,0]
	v_mul_f32_e32 v120, v120, v152
	v_mul_f32_e32 v121, v121, v152
	v_mul_f32_e32 v122, v122, v152
	v_mul_f32_e32 v123, v123, v152
	ds_write_b32 v103, v120 offset:0
	ds_write_b32 v103, v121 offset:4
	ds_write_b32 v103, v122 offset:8
	ds_write_b32 v103, v123 offset:12
	v_pk_mul_f32 v[124:125], v[124:125], s[10:11] op_sel_hi:[1,0]
	v_pk_mul_f32 v[126:127], v[126:127], s[10:11] op_sel_hi:[1,0]
	v_mul_f32_e32 v124, v124, v153
	v_mul_f32_e32 v125, v125, v153
	v_mul_f32_e32 v126, v126, v153
	v_mul_f32_e32 v127, v127, v153
	ds_write_b32 v103, v124 offset:1056
	ds_write_b32 v103, v125 offset:1060
	ds_write_b32 v103, v126 offset:1064
	ds_write_b32 v103, v127 offset:1068
	global_load_dwordx4 v[128:131], v102, s[56:57]
	s_add_u32 s56, s56, 0x10000
	s_addc_u32 s57, s57, 0
	global_load_dwordx4 v[132:135], v102, s[56:57]
	s_add_u32 s56, s56, 0x10000
	s_addc_u32 s57, s57, 0
	s_waitcnt vmcnt(1)
	v_pk_mul_f32 v[128:129], v[128:129], s[10:11] op_sel_hi:[1,0]
	v_pk_mul_f32 v[130:131], v[130:131], s[10:11] op_sel_hi:[1,0]
	v_mul_f32_e32 v128, v128, v154
	v_mul_f32_e32 v129, v129, v154
	v_mul_f32_e32 v130, v130, v154
	v_mul_f32_e32 v131, v131, v154
	ds_write_b32 v103, v128 offset:2112
	ds_write_b32 v103, v129 offset:2116
	ds_write_b32 v103, v130 offset:2120
	ds_write_b32 v103, v131 offset:2124
	s_waitcnt vmcnt(0)
	v_pk_mul_f32 v[132:133], v[132:133], s[10:11] op_sel_hi:[1,0]
	v_pk_mul_f32 v[134:135], v[134:135], s[10:11] op_sel_hi:[1,0]
	v_mul_f32_e32 v132, v132, v155
	v_mul_f32_e32 v133, v133, v155
	v_mul_f32_e32 v134, v134, v155
	v_mul_f32_e32 v135, v135, v155
	ds_write_b32 v103, v132 offset:3168
	ds_write_b32 v103, v133 offset:3172
	ds_write_b32 v103, v134 offset:3176
	ds_write_b32 v103, v135 offset:3180
	global_load_dwordx4 v[136:139], v102, s[56:57]
	s_add_u32 s56, s56, 0x10000
	s_addc_u32 s57, s57, 0
	global_load_dwordx4 v[140:143], v102, s[56:57]
	s_add_u32 s56, s56, 0x10000
	s_addc_u32 s57, s57, 0
	s_waitcnt vmcnt(1)
	v_pk_mul_f32 v[136:137], v[136:137], s[10:11] op_sel_hi:[1,0]
	v_pk_mul_f32 v[138:139], v[138:139], s[10:11] op_sel_hi:[1,0]
	v_mul_f32_e32 v136, v136, v156
	v_mul_f32_e32 v137, v137, v156
	v_mul_f32_e32 v138, v138, v156
	v_mul_f32_e32 v139, v139, v156
	ds_write_b32 v103, v136 offset:4224
	ds_write_b32 v103, v137 offset:4228
	ds_write_b32 v103, v138 offset:4232
	ds_write_b32 v103, v139 offset:4236
	s_waitcnt vmcnt(0)
	v_pk_mul_f32 v[140:141], v[140:141], s[10:11] op_sel_hi:[1,0]
	v_pk_mul_f32 v[142:143], v[142:143], s[10:11] op_sel_hi:[1,0]
	v_mul_f32_e32 v140, v140, v157
	v_mul_f32_e32 v141, v141, v157
	v_mul_f32_e32 v142, v142, v157
	v_mul_f32_e32 v143, v143, v157
	ds_write_b32 v103, v140 offset:5280
	ds_write_b32 v103, v141 offset:5284
	ds_write_b32 v103, v142 offset:5288
	ds_write_b32 v103, v143 offset:5292
	global_load_dwordx4 v[144:147], v102, s[56:57]
	s_add_u32 s56, s56, 0x10000
	s_addc_u32 s57, s57, 0
	global_load_dwordx4 v[148:151], v102, s[56:57]
	s_add_u32 s56, s56, 0x10000
	s_addc_u32 s57, s57, 0
	s_waitcnt vmcnt(1)
	v_pk_mul_f32 v[144:145], v[144:145], s[10:11] op_sel_hi:[1,0]
	v_pk_mul_f32 v[146:147], v[146:147], s[10:11] op_sel_hi:[1,0]
	v_mul_f32_e32 v144, v144, v158
	v_mul_f32_e32 v145, v145, v158
	v_mul_f32_e32 v146, v146, v158
	v_mul_f32_e32 v147, v147, v158
	ds_write_b32 v103, v144 offset:6336
	ds_write_b32 v103, v145 offset:6340
	ds_write_b32 v103, v146 offset:6344
	ds_write_b32 v103, v147 offset:6348
	s_waitcnt vmcnt(0)
	v_pk_mul_f32 v[148:149], v[148:149], s[10:11] op_sel_hi:[1,0]
	v_pk_mul_f32 v[150:151], v[150:151], s[10:11] op_sel_hi:[1,0]
	v_mul_f32_e32 v148, v148, v159
	v_mul_f32_e32 v149, v149, v159
	v_mul_f32_e32 v150, v150, v159
	v_mul_f32_e32 v151, v151, v159
	ds_write_b32 v103, v148 offset:7392
	ds_write_b32 v103, v149 offset:7396
	ds_write_b32 v103, v150 offset:7400
	ds_write_b32 v103, v151 offset:7404
	s_waitcnt lgkmcnt(0)
	v_add_u32_e32 v12, 0x400, v7
	ds_read2_b32 v[22:23], v7 offset1:16
	ds_read2_b32 v[34:35], v7 offset0:33 offset1:49
	ds_read2_b32 v[38:39], v7 offset0:66 offset1:82
	ds_read2_b32 v[40:41], v7 offset0:99 offset1:115
	ds_read2_b32 v[42:43], v7 offset0:132 offset1:148
	ds_read2_b32 v[44:45], v7 offset0:165 offset1:181
	ds_read2_b32 v[46:47], v7 offset0:198 offset1:214
	ds_read2_b32 v[48:49], v7 offset0:231 offset1:247
	ds_read2_b32 v[50:51], v12 offset0:8 offset1:24
	ds_read2_b32 v[52:53], v12 offset0:41 offset1:57
	ds_read2_b32 v[54:55], v12 offset0:74 offset1:90
	ds_read2_b32 v[56:57], v12 offset0:107 offset1:123
	ds_read2_b32 v[58:59], v12 offset0:140 offset1:156
	ds_read2_b32 v[60:61], v12 offset0:173 offset1:189
	s_lshl_b64 s[4:5], s[8:9], 21
	ds_read2_b32 v[62:63], v12 offset0:206 offset1:222
	ds_read2_b32 v[64:65], v12 offset0:239 offset1:255
	s_add_u32 s4, s3, s4
	s_waitcnt lgkmcnt(14)
	v_cvt_pk_fp8_f32 v30, v22, v34
	s_waitcnt lgkmcnt(10)
	v_cvt_pk_fp8_f32 v31, v42, v44
	s_waitcnt lgkmcnt(6)
	v_cvt_pk_fp8_f32 v32, v50, v52
	s_waitcnt lgkmcnt(2)
	v_cvt_pk_fp8_f32 v33, v58, v60
	s_addc_u32 s5, s11, s5
	s_lshl_b32 s8, s20, 6
	s_lshl_b32 s20, s20, 2
	s_and_b32 s8, s8, 0x700
	s_and_b32 s20, s20, 0x80
	s_or_b32 s8, s8, s20
	s_and_b32 s7, s7, 0x60
	s_add_u32 s4, s4, s6
	v_or_b32_e32 v3, s7, v5
	v_cvt_pk_fp8_f32 v30, v38, v40 op_sel:[0,0,1]
	v_cvt_pk_fp8_f32 v31, v46, v48 op_sel:[0,0,1]
	v_cvt_pk_fp8_f32 v32, v54, v56 op_sel:[0,0,1]
	s_waitcnt lgkmcnt(0)
	v_cvt_pk_fp8_f32 v33, v62, v64 op_sel:[0,0,1]
	s_addc_u32 s5, s5, 0
	v_or_b32_e32 v3, s8, v3
	v_lshl_add_u64 v[18:19], s[4:5], 0, v[10:11]
	v_lshlrev_b32_e32 v12, 10, v3
	v_lshl_add_u64 v[66:67], v[18:19], 0, v[12:13]
	v_mov_b32_e32 v160, v30
	v_mov_b32_e32 v161, v31
	v_mov_b32_e32 v162, v32
	v_mov_b32_e32 v163, v33
	v_mov_b32_e32 v164, v66
	v_mov_b32_e32 v165, v67
	v_or_b32_e32 v3, s7, v21
	v_or_b32_e32 v3, s8, v3
	v_cvt_pk_fp8_f32 v30, v23, v35
	v_cvt_pk_fp8_f32 v31, v43, v45
	v_cvt_pk_fp8_f32 v32, v51, v53
	v_cvt_pk_fp8_f32 v33, v59, v61
	v_cvt_pk_fp8_f32 v30, v39, v41 op_sel:[0,0,1]
	v_cvt_pk_fp8_f32 v31, v47, v49 op_sel:[0,0,1]
	v_cvt_pk_fp8_f32 v32, v55, v57 op_sel:[0,0,1]
	v_cvt_pk_fp8_f32 v33, v63, v65 op_sel:[0,0,1]
	v_lshlrev_b32_e32 v12, 10, v3
	v_lshl_add_u64 v[18:19], v[18:19], 0, v[12:13]
	v_mov_b32_e32 v166, v30
	v_mov_b32_e32 v167, v31
	v_mov_b32_e32 v168, v32
	v_mov_b32_e32 v169, v33
	v_mov_b32_e32 v170, v18
	v_mov_b32_e32 v171, v19
	s_mov_b32 s60, 1
	s_waitcnt lgkmcnt(0)

.LBB0_31:
	s_cmp_lg_u32 s60, 0
	s_cbranch_scc0 .Lnoflush
	global_store_dwordx4 v[164:165], v[160:163], off
	global_store_dwordx4 v[170:171], v[166:169], off
